# combo12a + nt on the P0 fp8 weight-copy stores (transposes and expert-u conversion; written once, read phases later)
# speedup vs baseline: 1.0053x; 1.0027x over previous
.LBB0_31:
	ds_read2_b32 v[54:55], v38 offset1:65
	v_add_u32_e32 v53, 0x400, v38
	ds_read2_b32 v[56:57], v53 offset0:4 offset1:69
	ds_read2_b32 v[58:59], v38 offset0:130 offset1:195
	ds_read2_b32 v[60:61], v53 offset0:134 offset1:199
	s_mul_hi_i32 s8, s31, 0x2aaaaaab
	s_waitcnt lgkmcnt(3)
	v_mul_f32_e32 v62, 0x42800000, v54
	v_mul_f32_e32 v55, 0x42800000, v55
	v_mov_b32_e32 v54, 0
	v_cvt_pk_fp8_f32 v54, v62, v55
	s_waitcnt lgkmcnt(2)
	v_mul_f32_e32 v53, 0x42800000, v56
	v_mul_f32_e32 v56, 0x42800000, v57
	v_mov_b32_e32 v55, 0
	v_cvt_pk_fp8_f32 v55, v53, v56
	v_add_u32_e32 v53, 0x800, v38
	s_waitcnt lgkmcnt(1)
	v_mul_f32_e32 v58, 0x42800000, v58
	v_mul_f32_e32 v59, 0x42800000, v59
	ds_read2_b32 v[56:57], v53 offset0:8 offset1:73
	v_add_u32_e32 v62, 0xc00, v38
	v_cvt_pk_fp8_f32 v54, v58, v59 op_sel:[0,0,1]
	ds_read2_b32 v[58:59], v62 offset0:12 offset1:77
	s_waitcnt lgkmcnt(2)
	v_mul_f32_e32 v60, 0x42800000, v60
	v_mul_f32_e32 v61, 0x42800000, v61
	v_cvt_pk_fp8_f32 v55, v60, v61 op_sel:[0,0,1]
	s_waitcnt lgkmcnt(1)
	v_mul_f32_e32 v64, 0x42800000, v56
	ds_read2_b32 v[60:61], v53 offset0:138 offset1:203
	ds_read2_b32 v[62:63], v62 offset0:142 offset1:207
	v_mul_f32_e32 v57, 0x42800000, v57
	v_mov_b32_e32 v56, 0
	s_waitcnt lgkmcnt(2)
	v_mul_f32_e32 v53, 0x42800000, v58
	v_mul_f32_e32 v58, 0x42800000, v59
	v_cvt_pk_fp8_f32 v56, v64, v57
	v_mov_b32_e32 v57, 0
	v_cvt_pk_fp8_f32 v57, v53, v58
	v_add_u32_e32 v53, 0x1000, v38
	ds_read2_b32 v[58:59], v53 offset0:16 offset1:81
	s_waitcnt lgkmcnt(2)
	v_mul_f32_e32 v60, 0x42800000, v60
	v_mul_f32_e32 v61, 0x42800000, v61
	v_add_u32_e32 v64, 0x1400, v38
	v_cvt_pk_fp8_f32 v56, v60, v61 op_sel:[0,0,1]
	ds_read2_b32 v[60:61], v64 offset0:20 offset1:85
	s_waitcnt lgkmcnt(2)
	v_mul_f32_e32 v62, 0x42800000, v62
	v_mul_f32_e32 v63, 0x42800000, v63
	v_cvt_pk_fp8_f32 v57, v62, v63 op_sel:[0,0,1]
	s_waitcnt lgkmcnt(1)
	v_mul_f32_e32 v66, 0x42800000, v58
	ds_read2_b32 v[62:63], v53 offset0:146 offset1:211
	ds_read2_b32 v[64:65], v64 offset0:150 offset1:215
	v_mul_f32_e32 v59, 0x42800000, v59
	v_mov_b32_e32 v58, 0
	v_cvt_pk_fp8_f32 v58, v66, v59
	s_waitcnt lgkmcnt(2)
	v_mul_f32_e32 v53, 0x42800000, v60
	v_mul_f32_e32 v60, 0x42800000, v61
	v_mov_b32_e32 v59, 0
	v_cvt_pk_fp8_f32 v59, v53, v60
	v_add_u32_e32 v53, 0x1800, v38
	s_waitcnt lgkmcnt(1)
	v_mul_f32_e32 v62, 0x42800000, v62
	v_mul_f32_e32 v63, 0x42800000, v63
	ds_read2_b32 v[60:61], v53 offset0:24 offset1:89
	v_add_u32_e32 v66, 0x1c00, v38
	v_cvt_pk_fp8_f32 v58, v62, v63 op_sel:[0,0,1]
	ds_read2_b32 v[62:63], v66 offset0:28 offset1:93
	s_waitcnt lgkmcnt(2)
	v_mul_f32_e32 v64, 0x42800000, v64
	v_mul_f32_e32 v65, 0x42800000, v65
	v_cvt_pk_fp8_f32 v59, v64, v65 op_sel:[0,0,1]
	s_waitcnt lgkmcnt(1)
	v_mul_f32_e32 v68, 0x42800000, v60
	ds_read2_b32 v[64:65], v53 offset0:154 offset1:219
	ds_read2_b32 v[66:67], v66 offset0:158 offset1:223
	v_mul_f32_e32 v61, 0x42800000, v61
	v_mov_b32_e32 v60, 0
	s_waitcnt lgkmcnt(2)
	v_mul_f32_e32 v53, 0x42800000, v62
	v_mul_f32_e32 v62, 0x42800000, v63
	v_cvt_pk_fp8_f32 v60, v68, v61
	v_mov_b32_e32 v61, 0
	s_lshr_b32 s9, s8, 31
	s_ashr_i32 s8, s8, 5
	v_cvt_pk_fp8_f32 v61, v53, v62
	s_add_i32 s8, s8, s9
	s_mul_i32 s9, s8, 0xffffd000
	s_waitcnt lgkmcnt(1)
	v_mul_f32_e32 v63, 0x42800000, v64
	s_waitcnt lgkmcnt(0)
	v_mul_f32_e32 v64, 0x42800000, v66
	v_mul_f32_e32 v62, 0x42800000, v67
	s_add_i32 s9, s9, s10
	v_mul_f32_e32 v53, 0x42800000, v65
	v_cvt_pk_fp8_f32 v61, v64, v62 op_sel:[0,0,1]
	v_add_u32_e32 v62, s9, v37
	v_cvt_pk_fp8_f32 v60, v63, v53 op_sel:[0,0,1]
	v_ashrrev_i32_e32 v63, 31, v62
	v_lshlrev_b64 v[62:63], 12, v[62:63]
	s_lshl_b32 s8, s8, 8
	v_lshl_add_u64 v[62:63], s[4:5], 0, v[62:63]
	s_ashr_i32 s9, s8, 31
	v_lshl_add_u64 v[62:63], v[62:63], 0, s[8:9]
	v_lshl_add_u64 v[62:63], v[62:63], 0, v[32:33]
	s_andn2_b64 vcc, exec, s[6:7]
	s_mov_b32 s10, s30
	s_mov_b32 s31, s11
	global_store_dwordx4 v[62:63], v[54:57], off nt
	global_store_dwordx4 v[62:63], v[58:61], off offset:16 nt
	s_barrier
	s_cbranch_vccz .LBB0_36

.LBB0_38:
	ds_read2_b32 v[40:41], v38 offset1:65
	v_add_u32_e32 v46, 0x400, v38
	ds_read2_b32 v[42:43], v46 offset0:4 offset1:69
	ds_read2_b32 v[44:45], v38 offset0:130 offset1:195
	ds_read2_b32 v[46:47], v46 offset0:134 offset1:199
	v_add_u32_e32 v49, 0xc00, v38
	s_waitcnt lgkmcnt(3)
	v_mul_f32_e32 v48, 0x42800000, v40
	v_mul_f32_e32 v41, 0x42800000, v41
	v_mov_b32_e32 v40, 0
	v_cvt_pk_fp8_f32 v40, v48, v41
	s_waitcnt lgkmcnt(2)
	v_mul_f32_e32 v42, 0x42800000, v42
	v_mul_f32_e32 v43, 0x42800000, v43
	v_mov_b32_e32 v41, 0
	v_add_u32_e32 v48, 0x800, v38
	v_cvt_pk_fp8_f32 v41, v42, v43
	ds_read2_b32 v[42:43], v48 offset0:8 offset1:73
	s_waitcnt lgkmcnt(2)
	v_mul_f32_e32 v44, 0x42800000, v44
	v_mul_f32_e32 v45, 0x42800000, v45
	v_cvt_pk_fp8_f32 v40, v44, v45 op_sel:[0,0,1]
	ds_read2_b32 v[44:45], v49 offset0:12 offset1:77
	s_waitcnt lgkmcnt(2)
	v_mul_f32_e32 v46, 0x42800000, v46
	v_mul_f32_e32 v47, 0x42800000, v47
	v_cvt_pk_fp8_f32 v41, v46, v47 op_sel:[0,0,1]
	s_waitcnt lgkmcnt(1)
	v_mul_f32_e32 v50, 0x42800000, v42
	ds_read2_b32 v[46:47], v48 offset0:138 offset1:203
	ds_read2_b32 v[48:49], v49 offset0:142 offset1:207
	v_mul_f32_e32 v43, 0x42800000, v43
	v_mov_b32_e32 v42, 0
	v_cvt_pk_fp8_f32 v42, v50, v43
	s_waitcnt lgkmcnt(2)
	v_mul_f32_e32 v44, 0x42800000, v44
	v_mul_f32_e32 v45, 0x42800000, v45
	v_mov_b32_e32 v43, 0
	v_add_u32_e32 v50, 0x1000, v38
	v_cvt_pk_fp8_f32 v43, v44, v45
	ds_read2_b32 v[44:45], v50 offset0:16 offset1:81
	s_waitcnt lgkmcnt(2)
	v_mul_f32_e32 v46, 0x42800000, v46
	v_mul_f32_e32 v47, 0x42800000, v47
	v_add_u32_e32 v51, 0x1400, v38
	v_cvt_pk_fp8_f32 v42, v46, v47 op_sel:[0,0,1]
	ds_read2_b32 v[46:47], v51 offset0:20 offset1:85
	s_waitcnt lgkmcnt(2)
	v_mul_f32_e32 v48, 0x42800000, v48
	v_mul_f32_e32 v49, 0x42800000, v49
	v_cvt_pk_fp8_f32 v43, v48, v49 op_sel:[0,0,1]
	s_waitcnt lgkmcnt(1)
	v_mul_f32_e32 v52, 0x42800000, v44
	ds_read2_b32 v[48:49], v50 offset0:146 offset1:211
	ds_read2_b32 v[50:51], v51 offset0:150 offset1:215
	v_mul_f32_e32 v45, 0x42800000, v45
	v_mov_b32_e32 v44, 0
	v_cvt_pk_fp8_f32 v44, v52, v45
	s_waitcnt lgkmcnt(2)
	v_mul_f32_e32 v46, 0x42800000, v46
	v_mul_f32_e32 v47, 0x42800000, v47
	v_mov_b32_e32 v45, 0
	v_add_u32_e32 v52, 0x1800, v38
	v_cvt_pk_fp8_f32 v45, v46, v47
	ds_read2_b32 v[46:47], v52 offset0:24 offset1:89
	s_waitcnt lgkmcnt(2)
	v_mul_f32_e32 v48, 0x42800000, v48
	v_mul_f32_e32 v49, 0x42800000, v49
	v_add_u32_e32 v53, 0x1c00, v38
	v_cvt_pk_fp8_f32 v44, v48, v49 op_sel:[0,0,1]
	ds_read2_b32 v[48:49], v53 offset0:28 offset1:93
	s_waitcnt lgkmcnt(2)
	v_mul_f32_e32 v50, 0x42800000, v50
	v_mul_f32_e32 v51, 0x42800000, v51
	v_cvt_pk_fp8_f32 v45, v50, v51 op_sel:[0,0,1]
	s_waitcnt lgkmcnt(1)
	v_mul_f32_e32 v54, 0x42800000, v46
	ds_read2_b32 v[50:51], v52 offset0:154 offset1:219
	ds_read2_b32 v[52:53], v53 offset0:158 offset1:223
	v_mul_f32_e32 v47, 0x42800000, v47
	v_mov_b32_e32 v46, 0
	s_ashr_i32 s10, s29, 31
	v_cvt_pk_fp8_f32 v46, v54, v47
	s_lshr_b32 s10, s10, 26
	s_waitcnt lgkmcnt(2)
	v_mul_f32_e32 v48, 0x42800000, v48
	v_mul_f32_e32 v49, 0x42800000, v49
	v_mov_b32_e32 v47, 0
	s_add_i32 s10, s29, s10
	v_cvt_pk_fp8_f32 v47, v48, v49
	s_ashr_i32 s10, s10, 6
	s_waitcnt lgkmcnt(1)
	v_mul_f32_e32 v50, 0x42800000, v50
	v_mul_f32_e32 v48, 0x42800000, v51
	v_cvt_pk_fp8_f32 v46, v50, v48 op_sel:[0,0,1]
	v_add_u32_e32 v48, s2, v37
	s_lshl_b32 s2, s10, 12
	s_waitcnt lgkmcnt(0)
	v_mul_f32_e32 v52, 0x42800000, v52
	v_mul_f32_e32 v49, 0x42800000, v53
	v_subrev_u32_e32 v48, s2, v48
	v_cvt_pk_fp8_f32 v47, v52, v49 op_sel:[0,0,1]
	v_ashrrev_i32_e32 v49, 31, v48
	v_lshlrev_b64 v[48:49], 12, v[48:49]
	s_lshl_b32 s10, s10, 8
	v_lshl_add_u64 v[48:49], s[6:7], 0, v[48:49]
	s_ashr_i32 s11, s10, 31
	v_lshl_add_u64 v[48:49], v[48:49], 0, s[10:11]
	v_lshl_add_u64 v[48:49], v[48:49], 0, v[32:33]
	s_andn2_b64 vcc, exec, s[8:9]
	s_mov_b32 s2, s28
	s_mov_b32 s29, s3
	global_store_dwordx4 v[48:49], v[40:43], off nt
	global_store_dwordx4 v[48:49], v[44:47], off offset:16 nt
	s_barrier
	s_cbranch_vccz .LBB0_43

.LBB0_45:
	ds_read2_b32 v[42:43], v38 offset1:65
	v_add_u32_e32 v40, 0x400, v38
	ds_read2_b32 v[44:45], v40 offset0:4 offset1:69
	ds_read2_b32 v[46:47], v38 offset0:130 offset1:195
	ds_read2_b32 v[48:49], v40 offset0:134 offset1:199
	v_mov_b32_e32 v40, 0
	v_mov_b32_e32 v41, 0
	s_waitcnt lgkmcnt(3)
	v_cvt_pk_fp8_f32 v40, v42, v43
	v_add_u32_e32 v42, 0x800, v38
	s_waitcnt lgkmcnt(2)
	v_cvt_pk_fp8_f32 v41, v44, v45
	ds_read2_b32 v[44:45], v42 offset0:8 offset1:73
	v_add_u32_e32 v43, 0xc00, v38
	ds_read2_b32 v[50:51], v43 offset0:12 offset1:77
	ds_read2_b32 v[52:53], v42 offset0:138 offset1:203
	ds_read2_b32 v[54:55], v43 offset0:142 offset1:207
	v_mov_b32_e32 v42, 0
	s_waitcnt lgkmcnt(5)
	v_cvt_pk_fp8_f32 v40, v46, v47 op_sel:[0,0,1]
	s_waitcnt lgkmcnt(3)
	v_cvt_pk_fp8_f32 v42, v44, v45
	v_add_u32_e32 v44, 0x1000, v38
	ds_read2_b32 v[46:47], v44 offset0:16 offset1:81
	v_mov_b32_e32 v43, 0
	v_add_u32_e32 v45, 0x1400, v38
	s_waitcnt lgkmcnt(3)
	v_cvt_pk_fp8_f32 v43, v50, v51
	v_cvt_pk_fp8_f32 v41, v48, v49 op_sel:[0,0,1]
	s_waitcnt lgkmcnt(2)
	v_cvt_pk_fp8_f32 v42, v52, v53 op_sel:[0,0,1]
	ds_read2_b32 v[48:49], v45 offset0:20 offset1:85
	ds_read2_b32 v[50:51], v44 offset0:146 offset1:211
	ds_read2_b32 v[52:53], v45 offset0:150 offset1:215
	v_mov_b32_e32 v44, 0
	s_waitcnt lgkmcnt(3)
	v_cvt_pk_fp8_f32 v44, v46, v47
	v_mov_b32_e32 v45, 0
	v_add_u32_e32 v46, 0x1800, v38
	s_waitcnt lgkmcnt(2)
	v_cvt_pk_fp8_f32 v45, v48, v49
	ds_read2_b32 v[48:49], v46 offset0:24 offset1:89
	s_ashr_i32 s10, s28, 31
	v_add_u32_e32 v47, 0x1c00, v38
	s_lshr_b32 s10, s10, 26
	v_cvt_pk_fp8_f32 v43, v54, v55 op_sel:[0,0,1]
	ds_read2_b32 v[54:55], v47 offset0:28 offset1:93
	ds_read2_b32 v[56:57], v46 offset0:154 offset1:219
	ds_read2_b32 v[58:59], v47 offset0:158 offset1:223
	s_add_i32 s10, s28, s10
	s_ashr_i32 s10, s10, 6
	v_mov_b32_e32 v46, 0
	v_mov_b32_e32 v47, 0
	s_waitcnt lgkmcnt(3)
	v_cvt_pk_fp8_f32 v46, v48, v49
	s_waitcnt lgkmcnt(2)
	v_cvt_pk_fp8_f32 v47, v54, v55
	v_add_u32_e32 v48, s3, v37
	s_lshl_b32 s3, s10, 12
	v_subrev_u32_e32 v48, s3, v48
	v_ashrrev_i32_e32 v49, 31, v48
	v_lshlrev_b64 v[48:49], 14, v[48:49]
	s_lshl_b32 s10, s10, 8
	v_cvt_pk_fp8_f32 v44, v50, v51 op_sel:[0,0,1]
	v_cvt_pk_fp8_f32 v45, v52, v53 op_sel:[0,0,1]
	s_waitcnt lgkmcnt(1)
	v_cvt_pk_fp8_f32 v46, v56, v57 op_sel:[0,0,1]
	s_waitcnt lgkmcnt(0)
	v_cvt_pk_fp8_f32 v47, v58, v59 op_sel:[0,0,1]
	v_lshl_add_u64 v[48:49], s[6:7], 0, v[48:49]
	s_ashr_i32 s11, s10, 31
	v_lshl_add_u64 v[48:49], v[48:49], 0, s[10:11]
	v_lshl_add_u64 v[48:49], v[48:49], 0, v[32:33]
	s_andn2_b64 vcc, exec, s[8:9]
	s_mov_b32 s3, s27
	s_mov_b32 s28, s26
	global_store_dwordx4 v[48:49], v[40:43], off nt
	global_store_dwordx4 v[48:49], v[44:47], off offset:16 nt
	s_barrier
	s_cbranch_vccz .LBB0_50

.LBB0_57:
	global_load_dwordx4 v[10:13], v[6:7], off offset:16
	global_load_dwordx4 v[14:17], v[6:7], off
	s_waitcnt vmcnt(5)
	v_lshl_add_u64 v[26:27], v[6:7], 0, s[14:15]
	v_lshl_add_u64 v[34:35], v[26:27], 0, s[14:15]
	v_lshl_add_u64 v[42:43], v[34:35], 0, s[14:15]
	global_load_dwordx4 v[18:21], v[26:27], off
	global_load_dwordx4 v[22:25], v[26:27], off offset:16
	s_nop 0
	global_load_dwordx4 v[26:29], v[34:35], off
	global_load_dwordx4 v[30:33], v[34:35], off offset:16
	s_nop 0
	global_load_dwordx4 v[34:37], v[42:43], off
	global_load_dwordx4 v[38:41], v[42:43], off offset:16
	v_lshl_add_u64 v[50:51], v[42:43], 0, s[14:15]
	global_load_dwordx4 v[42:45], v[50:51], off
	global_load_dwordx4 v[46:49], v[50:51], off offset:16
	v_lshl_add_u64 v[58:59], v[50:51], 0, s[14:15]
	global_load_dwordx4 v[50:53], v[58:59], off
	global_load_dwordx4 v[54:57], v[58:59], off offset:16
	v_lshl_add_u64 v[66:67], v[58:59], 0, s[14:15]
	global_load_dwordx4 v[58:61], v[66:67], off
	global_load_dwordx4 v[62:65], v[66:67], off offset:16
	v_lshl_add_u64 v[90:91], v[66:67], 0, s[14:15]
	global_load_dwordx4 v[66:69], v[90:91], off
	global_load_dwordx4 v[70:73], v[90:91], off offset:16
	v_mov_b32_e32 v8, 0
	v_mov_b32_e32 v9, 0
	v_mov_b32_e32 v74, 0
	v_mov_b32_e32 v75, 0
	v_mov_b32_e32 v79, 0
	v_mov_b32_e32 v81, 0
	s_add_u32 s0, s4, s4
	v_mov_b32_e32 v78, 0
	v_mov_b32_e32 v80, 0
	v_mov_b32_e32 v82, 0
	v_mov_b32_e32 v83, 0
	s_addc_u32 s1, s5, s5
	v_mov_b32_e32 v84, 0
	v_mov_b32_e32 v85, 0
	s_add_u32 s0, s0, s0
	v_mov_b32_e32 v86, 0
	v_mov_b32_e32 v87, 0
	s_addc_u32 s1, s1, s1
	v_lshl_add_u64 v[76:77], v[4:5], 0, s[26:27]
	v_mov_b32_e32 v88, 0
	v_mov_b32_e32 v89, 0
	s_add_u32 s0, s0, s0
	v_lshl_add_u64 v[90:91], v[76:77], 0, s[26:27]
	s_addc_u32 s1, s1, s1
	v_lshl_add_u64 v[92:93], v[90:91], 0, s[26:27]
	v_lshl_add_u64 v[2:3], s[0:1], 0, v[2:3]
	v_lshl_add_u64 v[94:95], v[92:93], 0, s[26:27]
	v_lshl_add_u64 v[102:103], s[8:9], 0, v[2:3]
	v_lshl_add_u64 v[96:97], v[94:95], 0, s[26:27]
	v_cmp_lt_u64_e32 vcc, s[30:31], v[102:103]
	v_lshl_add_u64 v[6:7], v[6:7], 0, s[12:13]
	v_lshl_add_u64 v[98:99], v[96:97], 0, s[26:27]
	s_or_b64 s[16:17], vcc, s[16:17]
	v_lshl_add_u64 v[100:101], v[98:99], 0, s[26:27]
	s_waitcnt vmcnt(15)
	v_pk_mul_f32 v[10:11], v[10:11], s[28:29] op_sel_hi:[1,0]
	s_waitcnt vmcnt(14)
	v_pk_mul_f32 v[14:15], v[14:15], s[28:29] op_sel_hi:[1,0]
	v_cvt_pk_fp8_f32 v9, v10, v11
	v_cvt_pk_fp8_f32 v8, v14, v15
	s_waitcnt vmcnt(13)
	v_pk_mul_f32 v[14:15], v[18:19], s[28:29] op_sel_hi:[1,0]
	v_pk_mul_f32 v[10:11], v[20:21], s[28:29] op_sel_hi:[1,0]
	s_waitcnt vmcnt(12)
	v_pk_mul_f32 v[18:19], v[24:25], s[28:29] op_sel_hi:[1,0]
	v_pk_mul_f32 v[20:21], v[22:23], s[28:29] op_sel_hi:[1,0]
	v_cvt_pk_fp8_f32 v74, v14, v15
	s_waitcnt vmcnt(11)
	v_pk_mul_f32 v[14:15], v[28:29], s[28:29] op_sel_hi:[1,0]
	s_waitcnt vmcnt(10)
	v_pk_mul_f32 v[24:25], v[30:31], s[28:29] op_sel_hi:[1,0]
	s_waitcnt vmcnt(8)
	v_pk_mul_f32 v[28:29], v[38:39], s[28:29] op_sel_hi:[1,0]
	v_pk_mul_f32 v[16:17], v[16:17], s[28:29] op_sel_hi:[1,0]
	v_cvt_pk_fp8_f32 v75, v20, v21
	v_pk_mul_f32 v[20:21], v[26:27], s[28:29] op_sel_hi:[1,0]
	v_pk_mul_f32 v[22:23], v[32:33], s[28:29] op_sel_hi:[1,0]
	v_cvt_pk_fp8_f32 v79, v24, v25
	v_pk_mul_f32 v[24:25], v[34:35], s[28:29] op_sel_hi:[1,0]
	v_cvt_pk_fp8_f32 v81, v28, v29
	s_waitcnt vmcnt(7)
	v_pk_mul_f32 v[28:29], v[42:43], s[28:29] op_sel_hi:[1,0]
	s_waitcnt vmcnt(6)
	v_pk_mul_f32 v[32:33], v[46:47], s[28:29] op_sel_hi:[1,0]
	v_cvt_pk_fp8_f32 v78, v20, v21
	v_cvt_pk_fp8_f32 v80, v24, v25
	v_cvt_pk_fp8_f32 v8, v16, v17 op_sel:[0,0,1]
	v_cvt_pk_fp8_f32 v82, v28, v29
	v_cvt_pk_fp8_f32 v83, v32, v33
	s_waitcnt vmcnt(5)
	v_pk_mul_f32 v[16:17], v[50:51], s[28:29] op_sel_hi:[1,0]
	s_waitcnt vmcnt(4)
	v_pk_mul_f32 v[32:33], v[54:55], s[28:29] op_sel_hi:[1,0]
	v_cvt_pk_fp8_f32 v84, v16, v17
	v_cvt_pk_fp8_f32 v85, v32, v33
	s_waitcnt vmcnt(3)
	v_pk_mul_f32 v[16:17], v[58:59], s[28:29] op_sel_hi:[1,0]
	s_waitcnt vmcnt(2)
	v_pk_mul_f32 v[32:33], v[62:63], s[28:29] op_sel_hi:[1,0]
	v_pk_mul_f32 v[12:13], v[12:13], s[28:29] op_sel_hi:[1,0]
	v_cvt_pk_fp8_f32 v86, v16, v17
	v_cvt_pk_fp8_f32 v87, v32, v33
	s_waitcnt vmcnt(1)
	v_pk_mul_f32 v[16:17], v[66:67], s[28:29] op_sel_hi:[1,0]
	s_waitcnt vmcnt(0)
	v_pk_mul_f32 v[32:33], v[70:71], s[28:29] op_sel_hi:[1,0]
	v_pk_mul_f32 v[20:21], v[36:37], s[28:29] op_sel_hi:[1,0]
	v_pk_mul_f32 v[26:27], v[40:41], s[28:29] op_sel_hi:[1,0]
	v_pk_mul_f32 v[24:25], v[44:45], s[28:29] op_sel_hi:[1,0]
	v_pk_mul_f32 v[30:31], v[48:49], s[28:29] op_sel_hi:[1,0]
	v_cvt_pk_fp8_f32 v9, v12, v13 op_sel:[0,0,1]
	v_cvt_pk_fp8_f32 v88, v16, v17
	v_cvt_pk_fp8_f32 v89, v32, v33
	v_pk_mul_f32 v[12:13], v[52:53], s[28:29] op_sel_hi:[1,0]
	v_pk_mul_f32 v[28:29], v[56:57], s[28:29] op_sel_hi:[1,0]
	v_cvt_pk_fp8_f32 v74, v10, v11 op_sel:[0,0,1]
	v_cvt_pk_fp8_f32 v75, v18, v19 op_sel:[0,0,1]
	v_cvt_pk_fp8_f32 v78, v14, v15 op_sel:[0,0,1]
	v_cvt_pk_fp8_f32 v79, v22, v23 op_sel:[0,0,1]
	v_cvt_pk_fp8_f32 v80, v20, v21 op_sel:[0,0,1]
	v_cvt_pk_fp8_f32 v81, v26, v27 op_sel:[0,0,1]
	v_cvt_pk_fp8_f32 v82, v24, v25 op_sel:[0,0,1]
	v_cvt_pk_fp8_f32 v83, v30, v31 op_sel:[0,0,1]
	v_pk_mul_f32 v[10:11], v[60:61], s[28:29] op_sel_hi:[1,0]
	v_pk_mul_f32 v[18:19], v[64:65], s[28:29] op_sel_hi:[1,0]
	v_cvt_pk_fp8_f32 v84, v12, v13 op_sel:[0,0,1]
	v_cvt_pk_fp8_f32 v85, v28, v29 op_sel:[0,0,1]
	v_pk_mul_f32 v[14:15], v[68:69], s[28:29] op_sel_hi:[1,0]
	v_pk_mul_f32 v[22:23], v[72:73], s[28:29] op_sel_hi:[1,0]
	v_cvt_pk_fp8_f32 v86, v10, v11 op_sel:[0,0,1]
	v_cvt_pk_fp8_f32 v87, v18, v19 op_sel:[0,0,1]
	global_store_dwordx2 v[4:5], v[8:9], off nt
	v_lshl_add_u64 v[4:5], v[4:5], 0, s[10:11]
	v_cvt_pk_fp8_f32 v88, v14, v15 op_sel:[0,0,1]
	v_cvt_pk_fp8_f32 v89, v22, v23 op_sel:[0,0,1]
	global_store_dwordx2 v[76:77], v[74:75], off nt
	global_store_dwordx2 v[90:91], v[78:79], off nt
	global_store_dwordx2 v[92:93], v[80:81], off nt
	global_store_dwordx2 v[94:95], v[82:83], off nt
	global_store_dwordx2 v[96:97], v[84:85], off nt
	global_store_dwordx2 v[98:99], v[86:87], off nt
	global_store_dwordx2 v[100:101], v[88:89], off nt
	s_andn2_b64 exec, exec, s[16:17]
	s_cbranch_execnz .LBB0_57
	s_or_b64 exec, exec, s[16:17]

.LBB0_61:
	global_load_dwordx4 v[8:11], v[4:5], off offset:-16
	global_load_dwordx4 v[12:15], v[4:5], off
	s_waitcnt vmcnt(7)
	v_mov_b32_e32 v16, 0
	v_mov_b32_e32 v17, 0
	v_lshl_add_u64 v[2:3], v[2:3], 0, s[4:5]
	v_cmp_lt_u64_e32 vcc, s[16:17], v[2:3]
	v_lshl_add_u64 v[4:5], v[4:5], 0, s[8:9]
	s_or_b64 s[12:13], vcc, s[12:13]
	s_waitcnt vmcnt(1)
	v_pk_mul_f32 v[8:9], v[8:9], s[14:15] op_sel_hi:[1,0]
	s_waitcnt vmcnt(0)
	v_pk_mul_f32 v[12:13], v[12:13], s[14:15] op_sel_hi:[1,0]
	v_cvt_pk_fp8_f32 v16, v8, v9
	v_cvt_pk_fp8_f32 v17, v12, v13
	v_pk_mul_f32 v[10:11], v[10:11], s[14:15] op_sel_hi:[1,0]
	v_pk_mul_f32 v[8:9], v[14:15], s[14:15] op_sel_hi:[1,0]
	v_cvt_pk_fp8_f32 v16, v10, v11 op_sel:[0,0,1]
	v_cvt_pk_fp8_f32 v17, v8, v9 op_sel:[0,0,1]
	global_store_dwordx2 v[6:7], v[16:17], off nt
	v_lshl_add_u64 v[6:7], v[6:7], 0, s[10:11]
	s_andn2_b64 exec, exec, s[12:13]
	s_cbranch_execnz .LBB0_61
